# v81 + in-projection and FFN-up K-loops: B-fragment LDS addresses via one base register and ds_read offsets (16 VALU per iteration removed)
# speedup vs baseline: 1.0048x; 1.0048x over previous
.LBB0_356:
	s_ashr_i32 s57, s56, 31
	s_lshl_b64 s[60:61], s[56:57], 19
	v_readlane_b32 s29, v253, 49
	s_add_u32 s60, s29, s60
	v_readlane_b32 s29, v253, 50
	s_addc_u32 s61, s29, s61
	s_and_b64 s[64:65], s[62:63], exec
	s_cselect_b32 s29, s61, s41
	s_cselect_b32 s37, s60, s40
	s_ashr_i32 s59, s58, 31
	s_lshl_b64 s[64:65], s[58:59], 19
	v_readlane_b32 s39, v253, 52
	s_add_u32 s64, s39, s64
	v_readlane_b32 s39, v253, 53
	s_addc_u32 s65, s39, s65
	s_and_b64 s[82:83], s[62:63], exec
	s_cselect_b32 s39, s65, s67
	s_cselect_b32 s57, s64, s66
	s_add_u32 s40, s40, 0x40080
	s_addc_u32 s41, s41, 0
	s_add_u32 s59, s66, 0x100
	v_mov_b32_e32 v2, 0
	s_addc_u32 vcc_lo, s67, 0
	s_mov_b32 vcc_hi, -2
	v_mov_b32_e32 v3, v2
	v_mov_b64_e32 v[4:5], v[2:3]
	v_mov_b64_e32 v[6:7], v[2:3]
	v_mov_b64_e32 v[8:9], v[2:3]
	v_mov_b64_e32 v[10:11], v[2:3]
	v_mov_b64_e32 v[12:13], v[2:3]
	v_mov_b64_e32 v[14:15], v[2:3]
	v_mov_b64_e32 v[16:17], v[2:3]
	v_mov_b64_e32 v[18:19], v[2:3]
	v_mov_b64_e32 v[20:21], v[2:3]
	v_mov_b64_e32 v[22:23], v[2:3]
	v_mov_b64_e32 v[24:25], v[2:3]
	v_mov_b64_e32 v[26:27], v[2:3]
	v_mov_b64_e32 v[28:29], v[2:3]
	v_mov_b64_e32 v[30:31], v[2:3]
	v_mov_b64_e32 v[32:33], v[2:3]
	v_mov_b64_e32 v[34:35], v[2:3]
	v_mov_b64_e32 v[36:37], v[2:3]
	v_mov_b64_e32 v[38:39], v[2:3]
	v_mov_b64_e32 v[40:41], v[2:3]
	v_mov_b64_e32 v[42:43], v[2:3]
	v_mov_b64_e32 v[44:45], v[2:3]
	v_mov_b64_e32 v[54:55], v[2:3]
	v_mov_b64_e32 v[56:57], v[2:3]
	v_mov_b64_e32 v[66:67], v[2:3]
	v_mov_b64_e32 v[68:69], v[2:3]
	v_mov_b64_e32 v[70:71], v[2:3]
	v_mov_b64_e32 v[72:73], v[2:3]
	v_mov_b64_e32 v[90:91], v[2:3]
	v_mov_b64_e32 v[92:93], v[2:3]
	v_mov_b64_e32 v[94:95], v[2:3]
	v_mov_b64_e32 v[96:97], v[2:3]
	v_mov_b64_e32 v[98:99], v[2:3]
	v_mov_b64_e32 v[100:101], v[2:3]
	v_mov_b64_e32 v[102:103], v[2:3]
	v_mov_b64_e32 v[104:105], v[2:3]
	v_mov_b64_e32 v[106:107], v[2:3]
	v_mov_b64_e32 v[108:109], v[2:3]
	v_mov_b64_e32 v[110:111], v[2:3]
	v_mov_b64_e32 v[112:113], v[2:3]
	v_mov_b64_e32 v[114:115], v[2:3]
	v_mov_b64_e32 v[116:117], v[2:3]
	v_mov_b64_e32 v[118:119], v[2:3]
	v_mov_b64_e32 v[120:121], v[2:3]
	v_mov_b64_e32 v[122:123], v[2:3]
	v_mov_b64_e32 v[124:125], v[2:3]
	v_mov_b64_e32 v[126:127], v[2:3]
	v_mov_b64_e32 v[128:129], v[2:3]
	v_mov_b64_e32 v[130:131], v[2:3]
	v_mov_b64_e32 v[132:133], v[2:3]
	v_mov_b64_e32 v[134:135], v[2:3]
	v_mov_b64_e32 v[136:137], v[2:3]
	v_mov_b64_e32 v[138:139], v[2:3]
	v_mov_b64_e32 v[140:141], v[2:3]
	v_mov_b64_e32 v[142:143], v[2:3]
	v_mov_b64_e32 v[144:145], v[2:3]
	v_mov_b64_e32 v[146:147], v[2:3]
	v_mov_b64_e32 v[148:149], v[2:3]
	v_mov_b64_e32 v[150:151], v[2:3]
	v_mov_b64_e32 v[152:153], v[2:3]
	v_mov_b64_e32 v[154:155], v[2:3]
	v_mov_b64_e32 v[156:157], v[2:3]
	v_mov_b64_e32 v[158:159], v[2:3]
	v_mov_b64_e32 v[160:161], v[2:3]
	v_add_u32_e32 v0, 0x10000, v220
.LBB0_357:
	ds_read_b128 v[46:49], v0
	ds_read_b128 v[50:53], v0 offset:1024
	ds_read_b128 v[58:61], v0 offset:2048
	ds_read_b128 v[62:65], v0 offset:3072
	ds_read_b128 v[74:77], v0 offset:16384
	ds_read_b128 v[78:81], v0 offset:17408
	ds_read_b128 v[82:85], v0 offset:18432
	ds_read_b128 v[86:89], v0 offset:19456
	s_add_u32 s50, s40, 0xfffc0080
	s_addc_u32 s51, s41, -1
	s_cmp_eq_u32 vcc_hi, 12
	s_cselect_b32 s83, s29, s51
	s_cselect_b32 s82, s37, s50
	s_cselect_b32 s67, s39, vcc_lo
	s_cselect_b32 s66, s57, s59
	s_add_i32 m0, s88, 0xc000
	ds_read_b128 v[192:195], v219
	ds_read_b128 v[200:203], v219 offset:1024
	ds_read_b128 v[204:207], v219 offset:2048
	ds_read_b128 v[208:211], v219 offset:3072
	ds_read_b128 v[212:215], v219 offset:4096
	ds_read_b128 v[236:239], v219 offset:5120
	ds_read_b128 v[240:243], v219 offset:6144
	ds_read_b128 v[244:247], v219 offset:7168
	global_load_lds_dwordx4 v170, s[40:41]
	s_add_i32 m0, s88, 0xe000
	s_nop 0
	global_load_lds_dwordx4 v172, s[40:41]
	s_waitcnt vmcnt(8)
	s_waitcnt lgkmcnt(0)
	s_barrier
	s_setprio 1
	s_waitcnt lgkmcnt(0)
	v_mfma_f32_16x16x32_bf16 v[158:161], v[46:49], v[192:195], v[158:161]
	v_mfma_f32_16x16x32_bf16 v[154:157], v[58:61], v[192:195], v[154:157]
	v_mfma_f32_16x16x32_bf16 v[142:145], v[46:49], v[204:207], v[142:145]
	v_mfma_f32_16x16x32_bf16 v[138:141], v[58:61], v[204:207], v[138:141]
	v_mfma_f32_16x16x32_bf16 v[126:129], v[46:49], v[212:215], v[126:129]
	v_mfma_f32_16x16x32_bf16 v[122:125], v[58:61], v[212:215], v[122:125]
	v_mfma_f32_16x16x32_bf16 v[110:113], v[46:49], v[240:243], v[110:113]
	v_mfma_f32_16x16x32_bf16 v[106:109], v[58:61], v[240:243], v[106:109]
	v_mfma_f32_16x16x32_bf16 v[158:161], v[50:53], v[200:203], v[158:161]
	v_mfma_f32_16x16x32_bf16 v[154:157], v[62:65], v[200:203], v[154:157]
	v_mfma_f32_16x16x32_bf16 v[142:145], v[50:53], v[208:211], v[142:145]
	v_mfma_f32_16x16x32_bf16 v[138:141], v[62:65], v[208:211], v[138:141]
	v_mfma_f32_16x16x32_bf16 v[126:129], v[50:53], v[236:239], v[126:129]
	v_mfma_f32_16x16x32_bf16 v[122:125], v[62:65], v[236:239], v[122:125]
	v_mfma_f32_16x16x32_bf16 v[110:113], v[50:53], v[244:247], v[110:113]
	v_mfma_f32_16x16x32_bf16 v[106:109], v[62:65], v[244:247], v[106:109]
	s_setprio 0
	s_setprio 1
	v_mfma_f32_16x16x32_bf16 v[150:153], v[74:77], v[192:195], v[150:153]
	v_mfma_f32_16x16x32_bf16 v[146:149], v[82:85], v[192:195], v[146:149]
	v_mfma_f32_16x16x32_bf16 v[134:137], v[74:77], v[204:207], v[134:137]
	v_mfma_f32_16x16x32_bf16 v[130:133], v[82:85], v[204:207], v[130:133]
	v_mfma_f32_16x16x32_bf16 v[118:121], v[74:77], v[212:215], v[118:121]
	v_mfma_f32_16x16x32_bf16 v[114:117], v[82:85], v[212:215], v[114:117]
	v_mfma_f32_16x16x32_bf16 v[102:105], v[74:77], v[240:243], v[102:105]
	v_mfma_f32_16x16x32_bf16 v[98:101], v[82:85], v[240:243], v[98:101]
	v_mfma_f32_16x16x32_bf16 v[150:153], v[78:81], v[200:203], v[150:153]
	v_mfma_f32_16x16x32_bf16 v[146:149], v[86:89], v[200:203], v[146:149]
	v_mfma_f32_16x16x32_bf16 v[134:137], v[78:81], v[208:211], v[134:137]
	v_mfma_f32_16x16x32_bf16 v[130:133], v[86:89], v[208:211], v[130:133]
	v_mfma_f32_16x16x32_bf16 v[118:121], v[78:81], v[236:239], v[118:121]
	v_mfma_f32_16x16x32_bf16 v[114:117], v[86:89], v[236:239], v[114:117]
	v_mfma_f32_16x16x32_bf16 v[102:105], v[78:81], v[244:247], v[102:105]
	v_mfma_f32_16x16x32_bf16 v[98:101], v[86:89], v[244:247], v[98:101]
	s_setprio 0
	s_barrier
	s_mov_b32 m0, s90
	s_add_u32 s50, s66, 0x40000
	ds_read_b128 v[192:195], v219 offset:16384
	ds_read_b128 v[200:203], v219 offset:17408
	ds_read_b128 v[204:207], v219 offset:18432
	ds_read_b128 v[208:211], v219 offset:19456
	ds_read_b128 v[212:215], v219 offset:20480
	ds_read_b128 v[236:239], v219 offset:21504
	ds_read_b128 v[240:243], v219 offset:22528
	ds_read_b128 v[244:247], v219 offset:23552
	global_load_lds_dwordx4 v166, s[66:67]
	v_lshl_add_u64 v[216:217], s[66:67], 0, v[162:163]
	s_mov_b32 m0, s91
	s_addc_u32 s51, s67, 0
	global_load_lds_dwordx4 v162, s[66:67]
	s_mov_b32 m0, s92
	s_nop 0
	global_load_lds_dwordx4 v166, s[50:51]
	s_mov_b32 m0, s93
	s_nop 0
	global_load_lds_dwordx4 v162, s[50:51]
	s_mov_b32 m0, s88
	s_nop 0
	global_load_lds_dwordx4 v168, s[82:83]
	s_mov_b32 m0, s94
	s_nop 0
	global_load_lds_dwordx4 v164, s[82:83]
	s_waitcnt vmcnt(8)
	s_waitcnt lgkmcnt(0)
	s_barrier
	s_setprio 1
	s_waitcnt lgkmcnt(0)
	v_mfma_f32_16x16x32_bf16 v[94:97], v[46:49], v[192:195], v[94:97]
	v_mfma_f32_16x16x32_bf16 v[90:93], v[58:61], v[192:195], v[90:93]
	v_mfma_f32_16x16x32_bf16 v[54:57], v[46:49], v[204:207], v[54:57]
	v_mfma_f32_16x16x32_bf16 v[42:45], v[58:61], v[204:207], v[42:45]
	v_mfma_f32_16x16x32_bf16 v[30:33], v[46:49], v[212:215], v[30:33]
	v_mfma_f32_16x16x32_bf16 v[26:29], v[58:61], v[212:215], v[26:29]
	v_mfma_f32_16x16x32_bf16 v[14:17], v[46:49], v[240:243], v[14:17]
	v_mfma_f32_16x16x32_bf16 v[10:13], v[58:61], v[240:243], v[10:13]
	v_mfma_f32_16x16x32_bf16 v[94:97], v[50:53], v[200:203], v[94:97]
	v_mfma_f32_16x16x32_bf16 v[90:93], v[62:65], v[200:203], v[90:93]
	v_mfma_f32_16x16x32_bf16 v[54:57], v[50:53], v[208:211], v[54:57]
	v_mfma_f32_16x16x32_bf16 v[42:45], v[62:65], v[208:211], v[42:45]
	v_mfma_f32_16x16x32_bf16 v[30:33], v[50:53], v[236:239], v[30:33]
	v_mfma_f32_16x16x32_bf16 v[26:29], v[62:65], v[236:239], v[26:29]
	v_mfma_f32_16x16x32_bf16 v[14:17], v[50:53], v[244:247], v[14:17]
	v_mfma_f32_16x16x32_bf16 v[10:13], v[62:65], v[244:247], v[10:13]
	s_setprio 0
	s_setprio 1
	v_mfma_f32_16x16x32_bf16 v[38:41], v[74:77], v[204:207], v[38:41]
	v_mfma_f32_16x16x32_bf16 v[34:37], v[82:85], v[204:207], v[34:37]
	v_mfma_f32_16x16x32_bf16 v[22:25], v[74:77], v[212:215], v[22:25]
	v_mfma_f32_16x16x32_bf16 v[18:21], v[82:85], v[212:215], v[18:21]
	v_mfma_f32_16x16x32_bf16 v[6:9], v[74:77], v[240:243], v[6:9]
	v_mfma_f32_16x16x32_bf16 v[2:5], v[82:85], v[240:243], v[2:5]
	v_mfma_f32_16x16x32_bf16 v[46:49], v[74:77], v[192:195], v[70:73]
	v_mfma_f32_16x16x32_bf16 v[50:53], v[82:85], v[192:195], v[66:69]
	v_mfma_f32_16x16x32_bf16 v[38:41], v[78:81], v[208:211], v[38:41]
	v_mfma_f32_16x16x32_bf16 v[34:37], v[86:89], v[208:211], v[34:37]
	v_mfma_f32_16x16x32_bf16 v[22:25], v[78:81], v[236:239], v[22:25]
	v_mfma_f32_16x16x32_bf16 v[18:21], v[86:89], v[236:239], v[18:21]
	v_mfma_f32_16x16x32_bf16 v[6:9], v[78:81], v[244:247], v[6:9]
	v_mfma_f32_16x16x32_bf16 v[2:5], v[86:89], v[244:247], v[2:5]
	v_mfma_f32_16x16x32_bf16 v[46:49], v[78:81], v[200:203], v[46:49]
	v_mfma_f32_16x16x32_bf16 v[50:53], v[86:89], v[200:203], v[50:53]
	s_setprio 0
	s_barrier
	ds_read_b128 v[58:61], v0 offset:32768
	ds_read_b128 v[62:65], v0 offset:33792
	ds_read_b128 v[66:69], v0 offset:34816
	ds_read_b128 v[70:73], v0 offset:35840
	ds_read_b128 v[74:77], v0 offset:49152
	ds_read_b128 v[78:81], v0 offset:50176
	ds_read_b128 v[82:85], v0 offset:51200
	ds_read_b128 v[86:89], v0 offset:52224
	s_add_u32 s50, s82, 0x40000
	s_addc_u32 s51, s83, 0
	s_mov_b32 m0, s95
	ds_read_b128 v[192:195], v219 offset:32768
	ds_read_b128 v[200:203], v219 offset:33792
	ds_read_b128 v[204:207], v219 offset:34816
	ds_read_b128 v[208:211], v219 offset:35840
	ds_read_b128 v[212:215], v219 offset:36864
	ds_read_b128 v[236:239], v219 offset:37888
	ds_read_b128 v[240:243], v219 offset:38912
	ds_read_b128 v[244:247], v219 offset:39936
	global_load_lds_dwordx4 v168, s[50:51]
	s_mov_b32 m0, s0
	s_nop 0
	global_load_lds_dwordx4 v164, s[50:51]
	s_waitcnt vmcnt(8)
	s_waitcnt lgkmcnt(0)
	s_barrier
	s_setprio 1
	s_waitcnt lgkmcnt(0)
	v_mfma_f32_16x16x32_bf16 v[158:161], v[58:61], v[192:195], v[158:161]
	v_mfma_f32_16x16x32_bf16 v[154:157], v[66:69], v[192:195], v[154:157]
	v_mfma_f32_16x16x32_bf16 v[142:145], v[58:61], v[204:207], v[142:145]
	v_mfma_f32_16x16x32_bf16 v[138:141], v[66:69], v[204:207], v[138:141]
	v_mfma_f32_16x16x32_bf16 v[126:129], v[58:61], v[212:215], v[126:129]
	v_mfma_f32_16x16x32_bf16 v[122:125], v[66:69], v[212:215], v[122:125]
	v_mfma_f32_16x16x32_bf16 v[110:113], v[58:61], v[240:243], v[110:113]
	v_mfma_f32_16x16x32_bf16 v[106:109], v[66:69], v[240:243], v[106:109]
	v_mfma_f32_16x16x32_bf16 v[158:161], v[62:65], v[200:203], v[158:161]
	v_mfma_f32_16x16x32_bf16 v[154:157], v[70:73], v[200:203], v[154:157]
	v_mfma_f32_16x16x32_bf16 v[142:145], v[62:65], v[208:211], v[142:145]
	v_mfma_f32_16x16x32_bf16 v[138:141], v[70:73], v[208:211], v[138:141]
	v_mfma_f32_16x16x32_bf16 v[126:129], v[62:65], v[236:239], v[126:129]
	v_mfma_f32_16x16x32_bf16 v[122:125], v[70:73], v[236:239], v[122:125]
	v_mfma_f32_16x16x32_bf16 v[110:113], v[62:65], v[244:247], v[110:113]
	v_mfma_f32_16x16x32_bf16 v[106:109], v[70:73], v[244:247], v[106:109]
	s_setprio 0
	s_setprio 1
	v_mfma_f32_16x16x32_bf16 v[150:153], v[74:77], v[192:195], v[150:153]
	v_mfma_f32_16x16x32_bf16 v[146:149], v[82:85], v[192:195], v[146:149]
	v_mfma_f32_16x16x32_bf16 v[134:137], v[74:77], v[204:207], v[134:137]
	v_mfma_f32_16x16x32_bf16 v[130:133], v[82:85], v[204:207], v[130:133]
	v_mfma_f32_16x16x32_bf16 v[118:121], v[74:77], v[212:215], v[118:121]
	v_mfma_f32_16x16x32_bf16 v[114:117], v[82:85], v[212:215], v[114:117]
	v_mfma_f32_16x16x32_bf16 v[102:105], v[74:77], v[240:243], v[102:105]
	v_mfma_f32_16x16x32_bf16 v[98:101], v[82:85], v[240:243], v[98:101]
	v_mfma_f32_16x16x32_bf16 v[150:153], v[78:81], v[200:203], v[150:153]
	v_mfma_f32_16x16x32_bf16 v[146:149], v[86:89], v[200:203], v[146:149]
	v_mfma_f32_16x16x32_bf16 v[134:137], v[78:81], v[208:211], v[134:137]
	v_mfma_f32_16x16x32_bf16 v[130:133], v[86:89], v[208:211], v[130:133]
	v_mfma_f32_16x16x32_bf16 v[118:121], v[78:81], v[236:239], v[118:121]
	v_mfma_f32_16x16x32_bf16 v[114:117], v[86:89], v[236:239], v[114:117]
	v_mfma_f32_16x16x32_bf16 v[102:105], v[78:81], v[244:247], v[102:105]
	v_mfma_f32_16x16x32_bf16 v[98:101], v[86:89], v[244:247], v[98:101]
	s_setprio 0
	s_barrier
	s_add_i32 m0, s1, 0xffffff80
	s_add_u32 s50, s66, 0x40080
	ds_read_b128 v[192:195], v219 offset:49152
	ds_read_b128 v[200:203], v219 offset:50176
	ds_read_b128 v[204:207], v219 offset:51200
	ds_read_b128 v[208:211], v219 offset:52224
	ds_read_b128 v[212:215], v219 offset:53248
	ds_read_b128 v[236:239], v219 offset:54272
	ds_read_b128 v[240:243], v219 offset:55296
	ds_read_b128 v[244:247], v219 offset:56320
	global_load_lds_dwordx4 v166, s[66:67] offset:128
	v_lshl_add_u64 v[182:183], v[216:217], 0, s[18:19]
	s_mov_b32 m0, s14
	s_addc_u32 s51, s67, 0
	global_load_lds_dwordx4 v[182:183], off
	s_mov_b32 m0, s34
	s_nop 0
	global_load_lds_dwordx4 v166, s[50:51]
	s_mov_b32 m0, s35
	s_nop 0
	global_load_lds_dwordx4 v162, s[50:51]
	s_add_i32 m0, s15, 0xffffff80
	s_nop 0
	global_load_lds_dwordx4 v168, s[82:83] offset:128
	s_add_i32 m0, s31, 0xffffff80
	s_nop 0
	global_load_lds_dwordx4 v164, s[82:83] offset:128
	s_waitcnt vmcnt(8)
	s_waitcnt lgkmcnt(0)
	s_barrier
	s_setprio 1
	s_waitcnt lgkmcnt(0)
	v_mfma_f32_16x16x32_bf16 v[94:97], v[58:61], v[192:195], v[94:97]
	v_mfma_f32_16x16x32_bf16 v[90:93], v[66:69], v[192:195], v[90:93]
	v_mfma_f32_16x16x32_bf16 v[54:57], v[58:61], v[204:207], v[54:57]
	v_mfma_f32_16x16x32_bf16 v[42:45], v[66:69], v[204:207], v[42:45]
	v_mfma_f32_16x16x32_bf16 v[30:33], v[58:61], v[212:215], v[30:33]
	v_mfma_f32_16x16x32_bf16 v[26:29], v[66:69], v[212:215], v[26:29]
	v_mfma_f32_16x16x32_bf16 v[14:17], v[58:61], v[240:243], v[14:17]
	v_mfma_f32_16x16x32_bf16 v[10:13], v[66:69], v[240:243], v[10:13]
	v_mfma_f32_16x16x32_bf16 v[94:97], v[62:65], v[200:203], v[94:97]
	v_mfma_f32_16x16x32_bf16 v[90:93], v[70:73], v[200:203], v[90:93]
	v_mfma_f32_16x16x32_bf16 v[54:57], v[62:65], v[208:211], v[54:57]
	v_mfma_f32_16x16x32_bf16 v[42:45], v[70:73], v[208:211], v[42:45]
	v_mfma_f32_16x16x32_bf16 v[30:33], v[62:65], v[236:239], v[30:33]
	v_mfma_f32_16x16x32_bf16 v[26:29], v[70:73], v[236:239], v[26:29]
	v_mfma_f32_16x16x32_bf16 v[14:17], v[62:65], v[244:247], v[14:17]
	v_mfma_f32_16x16x32_bf16 v[10:13], v[70:73], v[244:247], v[10:13]
	s_setprio 0
	s_setprio 1
	v_mfma_f32_16x16x32_bf16 v[46:49], v[74:77], v[192:195], v[46:49]
	v_mfma_f32_16x16x32_bf16 v[70:73], v[78:81], v[200:203], v[46:49]
	v_mfma_f32_16x16x32_bf16 v[46:49], v[82:85], v[192:195], v[50:53]
	v_mfma_f32_16x16x32_bf16 v[38:41], v[74:77], v[204:207], v[38:41]
	v_mfma_f32_16x16x32_bf16 v[34:37], v[82:85], v[204:207], v[34:37]
	v_mfma_f32_16x16x32_bf16 v[22:25], v[74:77], v[212:215], v[22:25]
	v_mfma_f32_16x16x32_bf16 v[18:21], v[82:85], v[212:215], v[18:21]
	v_mfma_f32_16x16x32_bf16 v[6:9], v[74:77], v[240:243], v[6:9]
	v_mfma_f32_16x16x32_bf16 v[2:5], v[82:85], v[240:243], v[2:5]
	v_mfma_f32_16x16x32_bf16 v[66:69], v[86:89], v[200:203], v[46:49]
	v_mfma_f32_16x16x32_bf16 v[38:41], v[78:81], v[208:211], v[38:41]
	v_mfma_f32_16x16x32_bf16 v[34:37], v[86:89], v[208:211], v[34:37]
	v_mfma_f32_16x16x32_bf16 v[22:25], v[78:81], v[236:239], v[22:25]
	v_mfma_f32_16x16x32_bf16 v[18:21], v[86:89], v[236:239], v[18:21]
	v_mfma_f32_16x16x32_bf16 v[6:9], v[78:81], v[244:247], v[6:9]
	v_mfma_f32_16x16x32_bf16 v[2:5], v[86:89], v[244:247], v[2:5]
	s_setprio 0
	s_barrier
	s_add_i32 vcc_hi, vcc_hi, 2
	s_add_u32 s40, s40, 0x100
	s_addc_u32 s41, s41, 0
	s_add_u32 s59, s59, 0x100
	s_addc_u32 vcc_lo, vcc_lo, 0
	s_cmp_gt_u32 vcc_hi, 13
	s_cbranch_scc0 .LBB0_357
	v_readlane_b32 s40, v253, 55
	v_readlane_b32 s41, v253, 56
	s_and_b64 vcc, exec, s[40:41]
	s_cbranch_vccz .LBB0_360
	s_barrier

.LBB0_2005:
	s_ashr_i32 s47, s46, 31
	s_lshl_b64 s[52:53], s[46:47], 19
	v_readlane_b32 s40, v253, 34
	v_readlane_b32 s41, v253, 35
	s_add_u32 s52, s40, s52
	s_addc_u32 s53, s41, s53
	s_and_b64 s[56:57], s[54:55], exec
	s_cselect_b32 s29, s53, s37
	s_cselect_b32 s47, s52, s36
	s_ashr_i32 s49, s48, 31
	s_lshl_b64 s[56:57], s[48:49], 19
	s_add_u32 s56, s35, s56
	s_addc_u32 s57, s64, s57
	s_and_b64 s[62:63], s[54:55], exec
	s_cselect_b32 s49, s57, s61
	s_cselect_b32 s59, s56, s60
	s_add_u32 s36, s36, 0x40080
	s_addc_u32 s37, s37, 0
	s_add_u32 s80, s60, 0x100
	v_mov_b32_e32 v2, 0
	s_addc_u32 s95, s61, 0
	s_mov_b32 vcc_lo, -2
	v_mov_b32_e32 v3, v2
	v_mov_b64_e32 v[4:5], v[2:3]
	v_mov_b64_e32 v[6:7], v[2:3]
	v_mov_b64_e32 v[8:9], v[2:3]
	v_mov_b64_e32 v[10:11], v[2:3]
	v_mov_b64_e32 v[12:13], v[2:3]
	v_mov_b64_e32 v[14:15], v[2:3]
	v_mov_b64_e32 v[16:17], v[2:3]
	v_mov_b64_e32 v[18:19], v[2:3]
	v_mov_b64_e32 v[20:21], v[2:3]
	v_mov_b64_e32 v[22:23], v[2:3]
	v_mov_b64_e32 v[24:25], v[2:3]
	v_mov_b64_e32 v[26:27], v[2:3]
	v_mov_b64_e32 v[28:29], v[2:3]
	v_mov_b64_e32 v[30:31], v[2:3]
	v_mov_b64_e32 v[32:33], v[2:3]
	v_mov_b64_e32 v[34:35], v[2:3]
	v_mov_b64_e32 v[36:37], v[2:3]
	v_mov_b64_e32 v[38:39], v[2:3]
	v_mov_b64_e32 v[40:41], v[2:3]
	v_mov_b64_e32 v[42:43], v[2:3]
	v_mov_b64_e32 v[44:45], v[2:3]
	v_mov_b64_e32 v[46:47], v[2:3]
	v_mov_b64_e32 v[48:49], v[2:3]
	v_mov_b64_e32 v[50:51], v[2:3]
	v_mov_b64_e32 v[52:53], v[2:3]
	v_mov_b64_e32 v[54:55], v[2:3]
	v_mov_b64_e32 v[56:57], v[2:3]
	v_mov_b64_e32 v[58:59], v[2:3]
	v_mov_b64_e32 v[60:61], v[2:3]
	v_mov_b64_e32 v[62:63], v[2:3]
	v_mov_b64_e32 v[64:65], v[2:3]
	v_mov_b64_e32 v[66:67], v[2:3]
	v_mov_b64_e32 v[68:69], v[2:3]
	v_mov_b64_e32 v[70:71], v[2:3]
	v_mov_b64_e32 v[72:73], v[2:3]
	v_mov_b64_e32 v[74:75], v[2:3]
	v_mov_b64_e32 v[76:77], v[2:3]
	v_mov_b64_e32 v[78:79], v[2:3]
	v_mov_b64_e32 v[80:81], v[2:3]
	v_mov_b64_e32 v[82:83], v[2:3]
	v_mov_b64_e32 v[84:85], v[2:3]
	v_mov_b64_e32 v[86:87], v[2:3]
	v_mov_b64_e32 v[88:89], v[2:3]
	v_mov_b64_e32 v[90:91], v[2:3]
	v_mov_b64_e32 v[92:93], v[2:3]
	v_mov_b64_e32 v[94:95], v[2:3]
	v_mov_b64_e32 v[96:97], v[2:3]
	v_mov_b64_e32 v[98:99], v[2:3]
	v_mov_b64_e32 v[100:101], v[2:3]
	v_mov_b64_e32 v[102:103], v[2:3]
	v_mov_b64_e32 v[104:105], v[2:3]
	v_mov_b64_e32 v[106:107], v[2:3]
	v_mov_b64_e32 v[108:109], v[2:3]
	v_mov_b64_e32 v[110:111], v[2:3]
	v_mov_b64_e32 v[112:113], v[2:3]
	v_mov_b64_e32 v[114:115], v[2:3]
	v_mov_b64_e32 v[116:117], v[2:3]
	v_mov_b64_e32 v[118:119], v[2:3]
	v_mov_b64_e32 v[120:121], v[2:3]
	v_mov_b64_e32 v[122:123], v[2:3]
	v_mov_b64_e32 v[124:125], v[2:3]
	v_mov_b64_e32 v[126:127], v[2:3]
	v_mov_b64_e32 v[128:129], v[2:3]
	v_add_u32_e32 v0, 0x10000, v164
.LBB0_2006:
	ds_read_b128 v[158:161], v0
	ds_read_b128 v[166:169], v0 offset:1024
	ds_read_b128 v[170:173], v0 offset:2048
	ds_read_b128 v[174:177], v0 offset:3072
	ds_read_b128 v[178:181], v0 offset:16384
	ds_read_b128 v[182:185], v0 offset:17408
	ds_read_b128 v[186:189], v0 offset:18432
	ds_read_b128 v[190:193], v0 offset:19456
	s_add_u32 s40, s36, 0xfffc0080
	s_addc_u32 s41, s37, -1
	s_cmp_eq_u32 vcc_lo, 12
	s_cselect_b32 s63, s29, s41
	s_cselect_b32 s62, s47, s40
	s_cselect_b32 s61, s49, s95
	s_cselect_b32 s60, s59, s80
	s_add_i32 m0, s31, 0xc000
	ds_read_b128 v[200:203], v163
	ds_read_b128 v[204:207], v163 offset:1024
	ds_read_b128 v[208:211], v163 offset:2048
	ds_read_b128 v[212:215], v163 offset:3072
	ds_read_b128 v[216:219], v163 offset:4096
	ds_read_b128 v[220:223], v163 offset:5120
	ds_read_b128 v[236:239], v163 offset:6144
	ds_read_b128 v[240:243], v163 offset:7168
	global_load_lds_dwordx4 v138, s[36:37]
	s_add_i32 m0, s31, 0xe000
	s_nop 0
	global_load_lds_dwordx4 v140, s[36:37]
	s_waitcnt vmcnt(8)
	s_waitcnt lgkmcnt(0)
	s_barrier
	s_setprio 1
	s_waitcnt lgkmcnt(0)
	v_mfma_f32_16x16x32_bf16 v[126:129], v[158:161], v[200:203], v[126:129]
	v_mfma_f32_16x16x32_bf16 v[122:125], v[170:173], v[200:203], v[122:125]
	v_mfma_f32_16x16x32_bf16 v[114:117], v[158:161], v[208:211], v[114:117]
	v_mfma_f32_16x16x32_bf16 v[106:109], v[170:173], v[208:211], v[106:109]
	v_mfma_f32_16x16x32_bf16 v[98:101], v[158:161], v[216:219], v[98:101]
	v_mfma_f32_16x16x32_bf16 v[90:93], v[170:173], v[216:219], v[90:93]
	v_mfma_f32_16x16x32_bf16 v[82:85], v[158:161], v[236:239], v[82:85]
	v_mfma_f32_16x16x32_bf16 v[74:77], v[170:173], v[236:239], v[74:77]
	v_mfma_f32_16x16x32_bf16 v[126:129], v[166:169], v[204:207], v[126:129]
	v_mfma_f32_16x16x32_bf16 v[122:125], v[174:177], v[204:207], v[122:125]
	v_mfma_f32_16x16x32_bf16 v[114:117], v[166:169], v[212:215], v[114:117]
	v_mfma_f32_16x16x32_bf16 v[106:109], v[174:177], v[212:215], v[106:109]
	v_mfma_f32_16x16x32_bf16 v[98:101], v[166:169], v[220:223], v[98:101]
	v_mfma_f32_16x16x32_bf16 v[90:93], v[174:177], v[220:223], v[90:93]
	v_mfma_f32_16x16x32_bf16 v[82:85], v[166:169], v[240:243], v[82:85]
	v_mfma_f32_16x16x32_bf16 v[74:77], v[174:177], v[240:243], v[74:77]
	s_setprio 0
	s_setprio 1
	v_mfma_f32_16x16x32_bf16 v[118:121], v[178:181], v[200:203], v[118:121]
	v_mfma_f32_16x16x32_bf16 v[110:113], v[186:189], v[200:203], v[110:113]
	v_mfma_f32_16x16x32_bf16 v[102:105], v[178:181], v[208:211], v[102:105]
	v_mfma_f32_16x16x32_bf16 v[94:97], v[186:189], v[208:211], v[94:97]
	v_mfma_f32_16x16x32_bf16 v[86:89], v[178:181], v[216:219], v[86:89]
	v_mfma_f32_16x16x32_bf16 v[78:81], v[186:189], v[216:219], v[78:81]
	v_mfma_f32_16x16x32_bf16 v[70:73], v[178:181], v[236:239], v[70:73]
	v_mfma_f32_16x16x32_bf16 v[66:69], v[186:189], v[236:239], v[66:69]
	v_mfma_f32_16x16x32_bf16 v[118:121], v[182:185], v[204:207], v[118:121]
	v_mfma_f32_16x16x32_bf16 v[110:113], v[190:193], v[204:207], v[110:113]
	v_mfma_f32_16x16x32_bf16 v[102:105], v[182:185], v[212:215], v[102:105]
	v_mfma_f32_16x16x32_bf16 v[94:97], v[190:193], v[212:215], v[94:97]
	v_mfma_f32_16x16x32_bf16 v[86:89], v[182:185], v[220:223], v[86:89]
	v_mfma_f32_16x16x32_bf16 v[78:81], v[190:193], v[220:223], v[78:81]
	v_mfma_f32_16x16x32_bf16 v[70:73], v[182:185], v[240:243], v[70:73]
	v_mfma_f32_16x16x32_bf16 v[66:69], v[190:193], v[240:243], v[66:69]
	s_setprio 0
	s_barrier
	s_mov_b32 m0, s51
	s_add_u32 s40, s60, 0x40000
	ds_read_b128 v[200:203], v163 offset:16384
	ds_read_b128 v[204:207], v163 offset:17408
	ds_read_b128 v[208:211], v163 offset:18432
	ds_read_b128 v[212:215], v163 offset:19456
	ds_read_b128 v[216:219], v163 offset:20480
	ds_read_b128 v[220:223], v163 offset:21504
	ds_read_b128 v[236:239], v163 offset:22528
	ds_read_b128 v[240:243], v163 offset:23552
	global_load_lds_dwordx4 v132, s[60:61]
	v_lshl_add_u64 v[226:227], s[60:61], 0, v[136:137]
	s_mov_b32 m0, s65
	s_addc_u32 s41, s61, 0
	global_load_lds_dwordx4 v136, s[60:61]
	s_mov_b32 m0, s66
	s_nop 0
	global_load_lds_dwordx4 v132, s[40:41]
	s_mov_b32 m0, s67
	s_nop 0
	global_load_lds_dwordx4 v136, s[40:41]
	s_mov_b32 m0, s31
	s_nop 0
	global_load_lds_dwordx4 v130, s[62:63]
	s_mov_b32 m0, s82
	s_nop 0
	global_load_lds_dwordx4 v134, s[62:63]
	s_waitcnt vmcnt(8)
	s_waitcnt lgkmcnt(0)
	s_barrier
	s_setprio 1
	s_waitcnt lgkmcnt(0)
	v_mfma_f32_16x16x32_bf16 v[62:65], v[158:161], v[200:203], v[62:65]
	v_mfma_f32_16x16x32_bf16 v[58:61], v[170:173], v[200:203], v[58:61]
	v_mfma_f32_16x16x32_bf16 v[54:57], v[158:161], v[208:211], v[54:57]
	v_mfma_f32_16x16x32_bf16 v[46:49], v[170:173], v[208:211], v[46:49]
	v_mfma_f32_16x16x32_bf16 v[38:41], v[158:161], v[216:219], v[38:41]
	v_mfma_f32_16x16x32_bf16 v[30:33], v[170:173], v[216:219], v[30:33]
	v_mfma_f32_16x16x32_bf16 v[22:25], v[158:161], v[236:239], v[22:25]
	v_mfma_f32_16x16x32_bf16 v[14:17], v[170:173], v[236:239], v[14:17]
	v_mfma_f32_16x16x32_bf16 v[62:65], v[166:169], v[204:207], v[62:65]
	v_mfma_f32_16x16x32_bf16 v[58:61], v[174:177], v[204:207], v[58:61]
	v_mfma_f32_16x16x32_bf16 v[54:57], v[166:169], v[212:215], v[54:57]
	v_mfma_f32_16x16x32_bf16 v[46:49], v[174:177], v[212:215], v[46:49]
	v_mfma_f32_16x16x32_bf16 v[38:41], v[166:169], v[220:223], v[38:41]
	v_mfma_f32_16x16x32_bf16 v[30:33], v[174:177], v[220:223], v[30:33]
	v_mfma_f32_16x16x32_bf16 v[22:25], v[166:169], v[240:243], v[22:25]
	v_mfma_f32_16x16x32_bf16 v[14:17], v[174:177], v[240:243], v[14:17]
	s_setprio 0
	s_setprio 1
	v_mfma_f32_16x16x32_bf16 v[50:53], v[178:181], v[200:203], v[50:53]
	v_mfma_f32_16x16x32_bf16 v[42:45], v[186:189], v[200:203], v[42:45]
	v_mfma_f32_16x16x32_bf16 v[34:37], v[178:181], v[208:211], v[34:37]
	v_mfma_f32_16x16x32_bf16 v[26:29], v[186:189], v[208:211], v[26:29]
	v_mfma_f32_16x16x32_bf16 v[18:21], v[178:181], v[216:219], v[18:21]
	v_mfma_f32_16x16x32_bf16 v[10:13], v[186:189], v[216:219], v[10:13]
	v_mfma_f32_16x16x32_bf16 v[6:9], v[178:181], v[236:239], v[6:9]
	v_mfma_f32_16x16x32_bf16 v[2:5], v[186:189], v[236:239], v[2:5]
	v_mfma_f32_16x16x32_bf16 v[50:53], v[182:185], v[204:207], v[50:53]
	v_mfma_f32_16x16x32_bf16 v[42:45], v[190:193], v[204:207], v[42:45]
	v_mfma_f32_16x16x32_bf16 v[34:37], v[182:185], v[212:215], v[34:37]
	v_mfma_f32_16x16x32_bf16 v[26:29], v[190:193], v[212:215], v[26:29]
	v_mfma_f32_16x16x32_bf16 v[18:21], v[182:185], v[220:223], v[18:21]
	v_mfma_f32_16x16x32_bf16 v[10:13], v[190:193], v[220:223], v[10:13]
	v_mfma_f32_16x16x32_bf16 v[6:9], v[182:185], v[240:243], v[6:9]
	v_mfma_f32_16x16x32_bf16 v[2:5], v[190:193], v[240:243], v[2:5]
	s_setprio 0
	s_barrier
	ds_read_b128 v[158:161], v0 offset:32768
	ds_read_b128 v[166:169], v0 offset:33792
	ds_read_b128 v[170:173], v0 offset:34816
	ds_read_b128 v[174:177], v0 offset:35840
	ds_read_b128 v[178:181], v0 offset:49152
	ds_read_b128 v[182:185], v0 offset:50176
	ds_read_b128 v[186:189], v0 offset:51200
	ds_read_b128 v[190:193], v0 offset:52224
	s_add_u32 s40, s62, 0x40000
	s_addc_u32 s41, s63, 0
	s_mov_b32 m0, s83
	ds_read_b128 v[200:203], v163 offset:32768
	ds_read_b128 v[204:207], v163 offset:33792
	ds_read_b128 v[208:211], v163 offset:34816
	ds_read_b128 v[212:215], v163 offset:35840
	ds_read_b128 v[216:219], v163 offset:36864
	ds_read_b128 v[220:223], v163 offset:37888
	ds_read_b128 v[236:239], v163 offset:38912
	ds_read_b128 v[240:243], v163 offset:39936
	global_load_lds_dwordx4 v130, s[40:41]
	s_mov_b32 m0, s84
	s_nop 0
	global_load_lds_dwordx4 v134, s[40:41]
	s_waitcnt vmcnt(8)
	s_waitcnt lgkmcnt(0)
	s_barrier
	s_setprio 1
	s_waitcnt lgkmcnt(0)
	v_mfma_f32_16x16x32_bf16 v[126:129], v[158:161], v[200:203], v[126:129]
	v_mfma_f32_16x16x32_bf16 v[122:125], v[170:173], v[200:203], v[122:125]
	v_mfma_f32_16x16x32_bf16 v[114:117], v[158:161], v[208:211], v[114:117]
	v_mfma_f32_16x16x32_bf16 v[106:109], v[170:173], v[208:211], v[106:109]
	v_mfma_f32_16x16x32_bf16 v[98:101], v[158:161], v[216:219], v[98:101]
	v_mfma_f32_16x16x32_bf16 v[90:93], v[170:173], v[216:219], v[90:93]
	v_mfma_f32_16x16x32_bf16 v[82:85], v[158:161], v[236:239], v[82:85]
	v_mfma_f32_16x16x32_bf16 v[74:77], v[170:173], v[236:239], v[74:77]
	v_mfma_f32_16x16x32_bf16 v[126:129], v[166:169], v[204:207], v[126:129]
	v_mfma_f32_16x16x32_bf16 v[122:125], v[174:177], v[204:207], v[122:125]
	v_mfma_f32_16x16x32_bf16 v[114:117], v[166:169], v[212:215], v[114:117]
	v_mfma_f32_16x16x32_bf16 v[106:109], v[174:177], v[212:215], v[106:109]
	v_mfma_f32_16x16x32_bf16 v[98:101], v[166:169], v[220:223], v[98:101]
	v_mfma_f32_16x16x32_bf16 v[90:93], v[174:177], v[220:223], v[90:93]
	v_mfma_f32_16x16x32_bf16 v[82:85], v[166:169], v[240:243], v[82:85]
	v_mfma_f32_16x16x32_bf16 v[74:77], v[174:177], v[240:243], v[74:77]
	s_setprio 0
	s_setprio 1
	v_mfma_f32_16x16x32_bf16 v[118:121], v[178:181], v[200:203], v[118:121]
	v_mfma_f32_16x16x32_bf16 v[110:113], v[186:189], v[200:203], v[110:113]
	v_mfma_f32_16x16x32_bf16 v[102:105], v[178:181], v[208:211], v[102:105]
	v_mfma_f32_16x16x32_bf16 v[94:97], v[186:189], v[208:211], v[94:97]
	v_mfma_f32_16x16x32_bf16 v[86:89], v[178:181], v[216:219], v[86:89]
	v_mfma_f32_16x16x32_bf16 v[78:81], v[186:189], v[216:219], v[78:81]
	v_mfma_f32_16x16x32_bf16 v[70:73], v[178:181], v[236:239], v[70:73]
	v_mfma_f32_16x16x32_bf16 v[66:69], v[186:189], v[236:239], v[66:69]
	v_mfma_f32_16x16x32_bf16 v[118:121], v[182:185], v[204:207], v[118:121]
	v_mfma_f32_16x16x32_bf16 v[110:113], v[190:193], v[204:207], v[110:113]
	v_mfma_f32_16x16x32_bf16 v[102:105], v[182:185], v[212:215], v[102:105]
	v_mfma_f32_16x16x32_bf16 v[94:97], v[190:193], v[212:215], v[94:97]
	v_mfma_f32_16x16x32_bf16 v[86:89], v[182:185], v[220:223], v[86:89]
	v_mfma_f32_16x16x32_bf16 v[78:81], v[190:193], v[220:223], v[78:81]
	v_mfma_f32_16x16x32_bf16 v[70:73], v[182:185], v[240:243], v[70:73]
	v_mfma_f32_16x16x32_bf16 v[66:69], v[190:193], v[240:243], v[66:69]
	s_setprio 0
	s_barrier
	s_add_i32 m0, s88, 0xffffff80
	s_add_u32 s40, s60, 0x40080
	ds_read_b128 v[200:203], v163 offset:49152
	ds_read_b128 v[204:207], v163 offset:50176
	ds_read_b128 v[208:211], v163 offset:51200
	ds_read_b128 v[212:215], v163 offset:52224
	ds_read_b128 v[216:219], v163 offset:53248
	ds_read_b128 v[220:223], v163 offset:54272
	ds_read_b128 v[236:239], v163 offset:55296
	ds_read_b128 v[240:243], v163 offset:56320
	global_load_lds_dwordx4 v132, s[60:61] offset:128
	v_lshl_add_u64 v[194:195], v[226:227], 0, s[18:19]
	s_mov_b32 m0, s89
	s_addc_u32 s41, s61, 0
	global_load_lds_dwordx4 v[194:195], off
	s_mov_b32 m0, s92
	s_nop 0
	global_load_lds_dwordx4 v132, s[40:41]
	s_mov_b32 m0, s93
	s_nop 0
	global_load_lds_dwordx4 v136, s[40:41]
	s_add_i32 m0, s90, 0xffffff80
	s_nop 0
	global_load_lds_dwordx4 v130, s[62:63] offset:128
	s_add_i32 m0, s91, 0xffffff80
	s_nop 0
	global_load_lds_dwordx4 v134, s[62:63] offset:128
	s_waitcnt vmcnt(8)
	s_waitcnt lgkmcnt(0)
	s_barrier
	s_setprio 1
	s_waitcnt lgkmcnt(0)
	v_mfma_f32_16x16x32_bf16 v[62:65], v[158:161], v[200:203], v[62:65]
	v_mfma_f32_16x16x32_bf16 v[58:61], v[170:173], v[200:203], v[58:61]
	v_mfma_f32_16x16x32_bf16 v[54:57], v[158:161], v[208:211], v[54:57]
	v_mfma_f32_16x16x32_bf16 v[46:49], v[170:173], v[208:211], v[46:49]
	v_mfma_f32_16x16x32_bf16 v[38:41], v[158:161], v[216:219], v[38:41]
	v_mfma_f32_16x16x32_bf16 v[30:33], v[170:173], v[216:219], v[30:33]
	v_mfma_f32_16x16x32_bf16 v[22:25], v[158:161], v[236:239], v[22:25]
	v_mfma_f32_16x16x32_bf16 v[14:17], v[170:173], v[236:239], v[14:17]
	v_mfma_f32_16x16x32_bf16 v[62:65], v[166:169], v[204:207], v[62:65]
	v_mfma_f32_16x16x32_bf16 v[58:61], v[174:177], v[204:207], v[58:61]
	v_mfma_f32_16x16x32_bf16 v[54:57], v[166:169], v[212:215], v[54:57]
	v_mfma_f32_16x16x32_bf16 v[46:49], v[174:177], v[212:215], v[46:49]
	v_mfma_f32_16x16x32_bf16 v[38:41], v[166:169], v[220:223], v[38:41]
	v_mfma_f32_16x16x32_bf16 v[30:33], v[174:177], v[220:223], v[30:33]
	v_mfma_f32_16x16x32_bf16 v[22:25], v[166:169], v[240:243], v[22:25]
	v_mfma_f32_16x16x32_bf16 v[14:17], v[174:177], v[240:243], v[14:17]
	s_setprio 0
	s_setprio 1
	v_mfma_f32_16x16x32_bf16 v[50:53], v[178:181], v[200:203], v[50:53]
	v_mfma_f32_16x16x32_bf16 v[42:45], v[186:189], v[200:203], v[42:45]
	v_mfma_f32_16x16x32_bf16 v[34:37], v[178:181], v[208:211], v[34:37]
	v_mfma_f32_16x16x32_bf16 v[26:29], v[186:189], v[208:211], v[26:29]
	v_mfma_f32_16x16x32_bf16 v[18:21], v[178:181], v[216:219], v[18:21]
	v_mfma_f32_16x16x32_bf16 v[10:13], v[186:189], v[216:219], v[10:13]
	v_mfma_f32_16x16x32_bf16 v[6:9], v[178:181], v[236:239], v[6:9]
	v_mfma_f32_16x16x32_bf16 v[2:5], v[186:189], v[236:239], v[2:5]
	v_mfma_f32_16x16x32_bf16 v[50:53], v[182:185], v[204:207], v[50:53]
	v_mfma_f32_16x16x32_bf16 v[42:45], v[190:193], v[204:207], v[42:45]
	v_mfma_f32_16x16x32_bf16 v[34:37], v[182:185], v[212:215], v[34:37]
	v_mfma_f32_16x16x32_bf16 v[26:29], v[190:193], v[212:215], v[26:29]
	v_mfma_f32_16x16x32_bf16 v[18:21], v[182:185], v[220:223], v[18:21]
	v_mfma_f32_16x16x32_bf16 v[10:13], v[190:193], v[220:223], v[10:13]
	v_mfma_f32_16x16x32_bf16 v[6:9], v[182:185], v[240:243], v[6:9]
	v_mfma_f32_16x16x32_bf16 v[2:5], v[190:193], v[240:243], v[2:5]
	s_setprio 0
	s_barrier
	s_add_i32 vcc_lo, vcc_lo, 2
	s_add_u32 s36, s36, 0x100
	s_addc_u32 s37, s37, 0
	s_add_u32 s80, s80, 0x100
	s_addc_u32 s95, s95, 0
	s_cmp_gt_u32 vcc_lo, 13
	s_cbranch_scc0 .LBB0_2006
	s_and_b64 vcc, exec, s[16:17]
	s_cbranch_vccz .LBB0_2009
	s_barrier
